# gqa16 tile loop: no exps behind the first eight P.V MFMAs (the six unconstrained ones ride as second slot behind MFMAs 11-16)
# speedup vs baseline: 1.0012x; 1.0012x over previous
; #define SBAR() __builtin_amdgcn_sched_barrier(0)
; template <int LDQ, int LDK, int LDO>
; __device__ __forceinline__ void attn_gqa16_body(const bf16* __restrict__ Qb, const bf16* __restrict__ Kh, const bf16* __restrict__ Vh, bf16* __restrict__ Ob, int seq, char* lds, float mref) {
;     ...
;     HPACK();
;     __syncthreads();
;     const bool more = t + 1 < NT;
;     if (more) HQK((t + 1) & 1);
;     const int vb = vb0 + (t & 1) * (int)G16_V;
;     SBAR(); pv16<0>(o, vb, pb); SBAR();
.LBB0_650:
	s_add_i32 s17, s16, 1
	s_and_b32 s16, s16, 1
	s_and_b32 s46, 1, s17
	s_cmp_eq_u32 s46, 1
	s_cselect_b32 s85, s86, s84
	s_cselect_b32 s46, 0x4400, 0
	v_add_u32_e32 v189, s46, v182
	v_cvt_pk_bf16_f32 v124, v134, v138
	v_cvt_pk_bf16_f32 v125, v136, v140
	v_cvt_pk_bf16_f32 v128, v135, v139
	v_cvt_pk_bf16_f32 v129, v137, v141
	s_waitcnt vmcnt(2)
	s_barrier
	ds_read_b128 v[130:133], v189 offset:33280
	ds_read_b128 v[146:149], v189 offset:33344
	ds_read_b128 v[200:203], v189 offset:37632
	ds_read_b128 v[204:207], v189 offset:37696
	ds_read_b128 v[212:215], v189 offset:41984
	ds_read_b128 v[216:219], v189 offset:42048
	ds_read_b128 v[224:227], v189 offset:46336
	ds_read_b128 v[228:231], v189 offset:46400
	s_mov_b32 m0, s85
	s_nop 0
	global_load_lds_dwordx4 v253, s[74:75]
	s_add_i32 m0, s85, 0x400
	s_nop 0
	global_load_lds_dwordx4 v253, s[76:77]
	s_add_u32 s74, s74, 0x90000
	s_addc_u32 s75, s75, 0
	s_add_u32 s76, s76, 0x90000
	s_addc_u32 s77, s77, 0
	s_waitcnt lgkmcnt(7)
	v_mfma_f32_16x16x32_bf16 v[196:199], v[130:133], v[30:33], v[248:251]
	v_add_f32_e64 v134, v134, v138
	v_add_f32_e64 v135, v135, v139
	v_pk_add_f32 v[136:137], v[136:137], v[140:141]
	s_mul_i32 s46, s16, 0x4100
	v_mfma_f32_16x16x32_bf16 v[130:133], v[130:133], v[38:41], v[248:251]
	v_cvt_pk_bf16_f32 v114, v246, v152
	s_waitcnt lgkmcnt(5)
	v_mfma_f32_16x16x32_bf16 v[208:211], v[200:203], v[30:33], v[248:251]
	v_cvt_pk_bf16_f32 v115, v240, v160
	v_mfma_f32_16x16x32_bf16 v[200:203], v[200:203], v[38:41], v[248:251]
	v_cvt_pk_bf16_f32 v116, v168, v170
	s_waitcnt lgkmcnt(3)
	v_mfma_f32_16x16x32_bf16 v[220:223], v[212:215], v[30:33], v[248:251]
	v_cvt_pk_bf16_f32 v117, v242, v244
	v_mfma_f32_16x16x32_bf16 v[212:215], v[212:215], v[38:41], v[248:251]
	v_cvt_pk_bf16_f32 v118, v247, v153
	s_waitcnt lgkmcnt(1)
	v_mfma_f32_16x16x32_bf16 v[232:235], v[224:227], v[30:33], v[248:251]
	v_cvt_pk_bf16_f32 v119, v241, v161
	v_mfma_f32_16x16x32_bf16 v[224:227], v[224:227], v[38:41], v[248:251]
	v_cvt_pk_bf16_f32 v120, v169, v171
	v_mfma_f32_16x16x32_bf16 v[196:199], v[146:149], v[18:21], v[196:199]
	v_cvt_pk_bf16_f32 v121, v243, v245
	v_mfma_f32_16x16x32_bf16 v[130:133], v[146:149], v[22:25], v[130:133]
	v_cvt_pk_bf16_f32 v122, v142, v172
	v_mfma_f32_16x16x32_bf16 v[146:149], v[204:207], v[18:21], v[208:211]
	v_cvt_pk_bf16_f32 v123, v144, v174
	v_mfma_f32_16x16x32_bf16 v[200:203], v[204:207], v[22:25], v[200:203]
	v_cvt_pk_bf16_f32 v126, v143, v173
	v_mfma_f32_16x16x32_bf16 v[204:207], v[216:219], v[18:21], v[220:223]
	v_cvt_pk_bf16_f32 v127, v145, v175
	v_mfma_f32_16x16x32_bf16 v[208:211], v[216:219], v[22:25], v[212:215]
	s_waitcnt lgkmcnt(0)
	v_mfma_f32_16x16x32_bf16 v[216:219], v[228:231], v[22:25], v[224:227]
	ds_read_b128 v[220:223], v189 offset:33408
	s_nop 1
	ds_read_b128 v[224:227], v189 offset:33472
	v_mfma_f32_16x16x32_bf16 v[212:215], v[228:231], v[18:21], v[232:235]
	s_waitcnt lgkmcnt(1)
	v_mfma_f32_16x16x32_bf16 v[196:199], v[220:223], v[10:13], v[196:199]
	v_mfma_f32_16x16x32_bf16 v[130:133], v[220:223], v[14:17], v[130:133]
	ds_read_b128 v[220:223], v189 offset:37760
	ds_read_b128 v[228:231], v189 offset:37824
	s_waitcnt lgkmcnt(1)
	v_mfma_f32_16x16x32_bf16 v[146:149], v[220:223], v[10:13], v[146:149]
	v_mfma_f32_16x16x32_bf16 v[200:203], v[220:223], v[14:17], v[200:203]
	ds_read_b128 v[220:223], v189 offset:42112
	ds_read_b128 v[232:235], v189 offset:42176
	s_waitcnt lgkmcnt(1)
	v_mfma_f32_16x16x32_bf16 v[204:207], v[220:223], v[10:13], v[204:207]
	v_mfma_f32_16x16x32_bf16 v[208:211], v[220:223], v[14:17], v[208:211]
	ds_read_b128 v[220:223], v189 offset:46464
	ds_read_b128 v[236:239], v189 offset:46528
	v_add_u32_e32 v189, s46, v183
	s_waitcnt lgkmcnt(1)
	v_mfma_f32_16x16x32_bf16 v[212:215], v[220:223], v[10:13], v[212:215]
	v_mfma_f32_16x16x32_bf16 v[216:219], v[220:223], v[14:17], v[216:219]
	v_mfma_f32_16x16x32_bf16 v[220:223], v[224:227], v[6:9], v[130:133]
	s_nop 2
	v_add_f32_e64 v130, v246, v152
	v_add_f32_e64 v131, v247, v153
	v_pk_add_f32 v[132:133], v[240:241], v[160:161]
	v_pk_add_f32 v[152:153], v[168:169], v[170:171]
	v_pk_add_f32 v[156:157], v[242:243], v[244:245]
	v_pk_add_f32 v[158:159], v[142:143], v[172:173]
	v_pk_add_f32 v[160:161], v[144:145], v[174:175]
	v_pk_add_f32 v[130:131], v[130:131], v[132:133]
	v_mfma_f32_16x16x32_bf16 v[142:145], v[232:235], v[2:5], v[204:207]
	v_add_f32_e64 v152, v152, v156
	v_add_f32_e64 v153, v153, v157
	v_pk_add_f32 v[156:157], v[158:159], v[160:161]
	v_pk_add_f32 v[158:159], v[134:135], v[136:137]
	v_mfma_f32_16x16x32_bf16 v[138:141], v[232:235], v[6:9], v[208:211]
	v_add_f32_e64 v150, v150, v130
	v_add_f32_e64 v151, v151, v131
	v_pk_add_f32 v[150:151], v[152:153], v[150:151]
	s_waitcnt lgkmcnt(0)
	v_mfma_f32_16x16x32_bf16 v[134:137], v[236:239], v[2:5], v[212:215]
	v_add_f32_e64 v150, v156, v150
	v_add_f32_e64 v151, v157, v151
	v_pk_add_f32 v[150:151], v[158:159], v[150:151]
	v_mfma_f32_16x16x32_bf16 v[196:199], v[224:227], v[2:5], v[196:199]
	v_mfma_f32_16x16x32_bf16 v[224:227], v[228:231], v[2:5], v[146:149]
	v_mfma_f32_16x16x32_bf16 v[146:149], v[228:231], v[6:9], v[200:203]
	v_mfma_f32_16x16x32_bf16 v[130:133], v[236:239], v[6:9], v[216:219]
	ds_read_b64_tr_b16 v[156:157], v189 offset:0
	ds_read_b64_tr_b16 v[158:159], v189 offset:0x200
	ds_read_b64_tr_b16 v[164:165], v189 offset:0x400
	ds_read_b64_tr_b16 v[166:167], v189 offset:0x600
	ds_read_b64_tr_b16 v[168:169], v189 offset:0x820
	ds_read_b64_tr_b16 v[170:171], v189 offset:0xa20
	ds_read_b64_tr_b16 v[172:173], v189 offset:0xc20
	ds_read_b64_tr_b16 v[174:175], v189 offset:0xe20
	ds_read_b64_tr_b16 v[200:201], v189 offset:0x1040
	ds_read_b64_tr_b16 v[202:203], v189 offset:0x1240
	ds_read_b64_tr_b16 v[204:205], v189 offset:0x1440
	ds_read_b64_tr_b16 v[206:207], v189 offset:0x1640
	s_waitcnt lgkmcnt(4)
; #define SBAR() __builtin_amdgcn_sched_barrier(0)
; #define MFMA16(a, b, c) __builtin_amdgcn_mfma_f32_16x16x32_bf16(a, b, c, 0, 0, 0)
; template <int D0> __device__ __forceinline__ void pv16(f32x4a (&o)[8][2], int vb, const bf16x8 (&pb)[2][2]) {
;     ...
;   const s16x4 a0 = TR(D0, 0, 0), a1 = TR(D0, 0, 1), a2 = TR(D0, 1, 0), a3 = TR(D0, 1, 1), b0 = TR(D0 + 1, 0, 0), b1 = TR(D0 + 1, 0, 1), b2 = TR(D0 + 1, 1, 0), b3 = TR(D0 + 1, 1, 1);
;   const s16x4 c0 = TR(D0 + 2, 0, 0), c1 = TR(D0 + 2, 0, 1), c2 = TR(D0 + 2, 1, 0), c3 = TR(D0 + 2, 1, 1);
;   asm volatile("s_waitcnt lgkmcnt(4)" ::: "memory"); SBAR();
;   o[D0][0] = MFMA16(PK16(a0, a1), pb[0][0], o[D0][0]); o[D0][1] = MFMA16(PK16(a0, a1), pb[0][1], o[D0][1]);
;   o[D0 + 1][0] = MFMA16(PK16(b0, b1), pb[0][0], o[D0 + 1][0]); o[D0 + 1][1] = MFMA16(PK16(b0, b1), pb[0][1], o[D0 + 1][1]);
;   o[D0][0] = MFMA16(PK16(a2, a3), pb[1][0], o[D0][0]); o[D0][1] = MFMA16(PK16(a2, a3), pb[1][1], o[D0][1]);
;   o[D0 + 1][0] = MFMA16(PK16(b2, b3), pb[1][0], o[D0 + 1][0]); o[D0 + 1][1] = MFMA16(PK16(b2, b3), pb[1][1], o[D0 + 1][1]);
;   SBAR();
;   const s16x4 d0 = TR(D0 + 3, 0, 0), d1 = TR(D0 + 3, 0, 1), d2 = TR(D0 + 3, 1, 0), d3 = TR(D0 + 3, 1, 1);
;   asm volatile("s_waitcnt lgkmcnt(4)" ::: "memory"); SBAR();
;   o[D0 + 2][0] = MFMA16(PK16(c0, c1), pb[0][0], o[D0 + 2][0]); o[D0 + 2][1] = MFMA16(PK16(c0, c1), pb[0][1], o[D0 + 2][1]);
;   o[D0 + 2][0] = MFMA16(PK16(c2, c3), pb[1][0], o[D0 + 2][0]); o[D0 + 2][1] = MFMA16(PK16(c2, c3), pb[1][1], o[D0 + 2][1]);
;   asm volatile("s_waitcnt lgkmcnt(0)" ::: "memory"); SBAR();
;   o[D0 + 3][0] = MFMA16(PK16(d0, d1), pb[0][0], o[D0 + 3][0]); o[D0 + 3][1] = MFMA16(PK16(d0, d1), pb[0][1], o[D0 + 3][1]);
;   o[D0 + 3][0] = MFMA16(PK16(d2, d3), pb[1][0], o[D0 + 3][0]); o[D0 + 3][1] = MFMA16(PK16(d2, d3), pb[1][1], o[D0 + 3][1]);
; template <int LDQ, int LDK, int LDO>
; __device__ __forceinline__ void attn_gqa16_body(const bf16* __restrict__ Qb, const bf16* __restrict__ Kh, const bf16* __restrict__ Vh, bf16* __restrict__ Ob, int seq, char* lds, float mref) {
;     ...
;     asm volatile("s_waitcnt vmcnt(0)" ::: "memory");
;     if (t + 2 < NT) HWRITEK(t & 1);
;     if (t + 1 < NT) HWRITEV((t + 1) & 1);
;     HLOADK(t + 3); HLOADV(t + 2);
;     SBAR(); pv16<4>(o, vb, pb); SBAR();
;     if (more) HEXP();
	s_nop 0
	v_mfma_f32_16x16x32_bf16 v[102:105], v[156:159], v[114:117], v[102:105]
	v_mfma_f32_16x16x32_bf16 v[98:101], v[156:159], v[118:121], v[98:101]
	v_mfma_f32_16x16x32_bf16 v[94:97], v[168:171], v[114:117], v[94:97]
	v_mfma_f32_16x16x32_bf16 v[90:93], v[168:171], v[118:121], v[90:93]
	v_mfma_f32_16x16x32_bf16 v[102:105], v[164:167], v[122:125], v[102:105]
	v_mfma_f32_16x16x32_bf16 v[98:101], v[164:167], v[126:129], v[98:101]
	v_mfma_f32_16x16x32_bf16 v[94:97], v[172:175], v[122:125], v[94:97]
	v_mfma_f32_16x16x32_bf16 v[90:93], v[172:175], v[126:129], v[90:93]
	ds_read_b64_tr_b16 v[156:157], v189 offset:0x1860
	ds_read_b64_tr_b16 v[158:159], v189 offset:0x1a60
	ds_read_b64_tr_b16 v[164:165], v189 offset:0x1c60
	ds_read_b64_tr_b16 v[166:167], v189 offset:0x1e60
	s_waitcnt lgkmcnt(4)
	v_mfma_f32_16x16x32_bf16 v[78:81], v[200:203], v[114:117], v[78:81]
	v_exp_f32_e32 v172, v143
	s_waitcnt lgkmcnt(0)
	v_mfma_f32_16x16x32_bf16 v[50:53], v[200:203], v[118:121], v[50:53]
	v_exp_f32_e32 v174, v145
	v_mfma_f32_16x16x32_bf16 v[78:81], v[204:207], v[122:125], v[78:81]
	v_exp_f32_e32 v246, v196
	v_exp_f32_e32 v143, v138
	v_mfma_f32_16x16x32_bf16 v[50:53], v[204:207], v[126:129], v[50:53]
	v_exp_f32_e32 v240, v198
	v_exp_f32_e32 v173, v139
	v_mfma_f32_16x16x32_bf16 v[82:85], v[156:159], v[114:117], v[82:85]
	v_exp_f32_e32 v160, v199
	v_exp_f32_e32 v145, v140
	v_mfma_f32_16x16x32_bf16 v[86:89], v[156:159], v[118:121], v[86:89]
	v_exp_f32_e32 v247, v220
	v_exp_f32_e32 v175, v141
	v_mfma_f32_16x16x32_bf16 v[82:85], v[164:167], v[122:125], v[82:85]
	v_exp_f32_e32 v241, v222
	v_exp_f32_e32 v138, v135
	v_mfma_f32_16x16x32_bf16 v[86:89], v[164:167], v[126:129], v[86:89]
	v_exp_f32_e32 v161, v223
	v_exp_f32_e32 v140, v137
	v_lshl_add_u64 v[152:153], v[162:163], 0, s[14:15]
	v_add_co_u32_e32 v156, vcc, s37, v152
	s_mulk_i32 s16, 0x4400
	s_nop 0
	v_addc_co_u32_e32 v157, vcc, 0, v153, vcc
	v_add_co_u32_e32 v158, vcc, s38, v152
	v_add_u32_e32 v164, s16, v194
	s_nop 0
	v_addc_co_u32_e32 v159, vcc, 0, v153, vcc
	s_waitcnt vmcnt(2)
	ds_write_b128 v164, v[106:109] offset:33280
	ds_write_b128 v164, v[110:113] offset:41984
	global_load_dwordx4 v[106:109], v[156:157], off offset:3072
	global_load_dwordx4 v[110:113], v[158:159], off offset:3072
	ds_read_b64_tr_b16 v[156:157], v189 offset:0x2080
	ds_read_b64_tr_b16 v[158:159], v189 offset:0x2280
	ds_read_b64_tr_b16 v[164:165], v189 offset:0x2480
	ds_read_b64_tr_b16 v[166:167], v189 offset:0x2680
	ds_read_b64_tr_b16 v[200:201], v189 offset:0x28a0
	ds_read_b64_tr_b16 v[202:203], v189 offset:0x2aa0
	ds_read_b64_tr_b16 v[204:205], v189 offset:0x2ca0
	ds_read_b64_tr_b16 v[206:207], v189 offset:0x2ea0
	s_waitcnt lgkmcnt(6)
	s_nop 0
	v_mfma_f32_16x16x32_bf16 v[54:57], v[156:159], v[114:117], v[54:57]
	v_exp_f32_e32 v135, v130
	v_mfma_f32_16x16x32_bf16 v[62:65], v[156:159], v[118:121], v[62:65]
	v_exp_f32_e32 v139, v131
	ds_read_b64_tr_b16 v[156:157], v189 offset:0x30c0
	ds_read_b64_tr_b16 v[158:159], v189 offset:0x32c0
	s_waitcnt lgkmcnt(4)
	v_mfma_f32_16x16x32_bf16 v[58:61], v[200:203], v[114:117], v[58:61]
	v_exp_f32_e32 v137, v132
	v_mfma_f32_16x16x32_bf16 v[70:73], v[200:203], v[118:121], v[70:73]
	v_exp_f32_e32 v141, v133
	ds_read_b64_tr_b16 v[200:201], v189 offset:0x38e0
	ds_read_b64_tr_b16 v[202:203], v189 offset:0x3ae0
	s_waitcnt lgkmcnt(6)
	v_mfma_f32_16x16x32_bf16 v[54:57], v[164:167], v[122:125], v[54:57]
	v_exp_f32_e32 v168, v224
	v_mfma_f32_16x16x32_bf16 v[62:65], v[164:167], v[126:129], v[62:65]
	v_exp_f32_e32 v170, v225
	ds_read_b64_tr_b16 v[164:165], v189 offset:0x34c0
	ds_read_b64_tr_b16 v[166:167], v189 offset:0x36c0
	s_waitcnt lgkmcnt(6)
	v_mfma_f32_16x16x32_bf16 v[58:61], v[204:207], v[122:125], v[58:61]
	v_exp_f32_e32 v169, v146
	v_mfma_f32_16x16x32_bf16 v[70:73], v[204:207], v[126:129], v[70:73]
	v_exp_f32_e32 v171, v147
	ds_read_b64_tr_b16 v[204:205], v189 offset:0x3ce0
	ds_read_b64_tr_b16 v[206:207], v189 offset:0x3ee0
	s_waitcnt lgkmcnt(6)
	v_mfma_f32_16x16x32_bf16 v[42:45], v[156:159], v[114:117], v[42:45]
	v_exp_f32_e32 v152, v197
	v_exp_f32_e32 v134, v134
	v_mfma_f32_16x16x32_bf16 v[46:49], v[156:159], v[118:121], v[46:49]
	v_exp_f32_e32 v153, v221
	v_exp_f32_e32 v136, v136
	s_waitcnt lgkmcnt(4)
	v_mfma_f32_16x16x32_bf16 v[66:69], v[200:203], v[114:117], v[66:69]
	v_exp_f32_e32 v242, v226
	v_mfma_f32_16x16x32_bf16 v[74:77], v[200:203], v[118:121], v[74:77]
	v_exp_f32_e32 v244, v227
	s_waitcnt lgkmcnt(2)
	v_mfma_f32_16x16x32_bf16 v[42:45], v[164:167], v[122:125], v[42:45]
	v_exp_f32_e32 v243, v148
	v_mfma_f32_16x16x32_bf16 v[46:49], v[164:167], v[126:129], v[46:49]
	v_exp_f32_e32 v245, v149
	s_waitcnt lgkmcnt(0)
	v_mfma_f32_16x16x32_bf16 v[66:69], v[204:207], v[122:125], v[66:69]
	v_exp_f32_e32 v142, v142
	v_mfma_f32_16x16x32_bf16 v[74:77], v[204:207], v[126:129], v[74:77]
	v_exp_f32_e32 v144, v144
	s_add_u32 s14, s14, 0x90000
	s_addc_u32 s15, s15, 0
	s_cmp_lg_u32 s14, 0x9120000
	s_mov_b32 s16, s17
	s_cbranch_scc1 .LBB0_650
	v_mov_b32_e32 v156, v240
	v_mov_b32_e32 v157, v241
	v_mov_b32_e32 v158, v246
	v_mov_b32_e32 v159, v247
	v_mov_b32_e32 v164, v242
	v_mov_b32_e32 v165, v243
	v_mov_b32_e32 v166, v244
	v_mov_b32_e32 v167, v245
	s_waitcnt vmcnt(1)
	v_cvt_pk_bf16_f32 v106, v158, v152
	v_cvt_pk_bf16_f32 v107, v156, v160
	v_cvt_pk_bf16_f32 v108, v168, v170
	v_cvt_pk_bf16_f32 v109, v164, v166
	s_waitcnt vmcnt(0)
	v_cvt_pk_bf16_f32 v110, v159, v153
	v_cvt_pk_bf16_f32 v111, v157, v161
	v_cvt_pk_bf16_f32 v112, v169, v171
	v_cvt_pk_bf16_f32 v113, v165, v167
	v_cvt_pk_bf16_f32 v114, v142, v172
	v_cvt_pk_bf16_f32 v115, v144, v174
	v_cvt_pk_bf16_f32 v116, v134, v138
	v_cvt_pk_bf16_f32 v117, v136, v140
	v_cvt_pk_bf16_f32 v118, v143, v173
	v_cvt_pk_bf16_f32 v119, v145, v175
	v_cvt_pk_bf16_f32 v120, v135, v139
	v_cvt_pk_bf16_f32 v121, v137, v141
	s_waitcnt lgkmcnt(0)
	s_barrier
; #define SBAR() __builtin_amdgcn_sched_barrier(0)
; template <int LDQ, int LDK, int LDO>
; __device__ __forceinline__ void attn_gqa16_body(const bf16* __restrict__ Qb, const bf16* __restrict__ Kh, const bf16* __restrict__ Vh, bf16* __restrict__ Ob, int seq, char* lds, float mref) {
;     ...
;   for (int t = 0; t < NT; ++t) {
;     HPACK();
;     __syncthreads();
;     const bool more = t + 1 < NT;
;     if (more) HQK((t + 1) & 1);
;     const int vb = vb0 + (t & 1) * (int)G16_V;
;     SBAR(); pv16<0>(o, vb, pb); SBAR();
	s_mov_b32 m0, s86
	s_nop 0
	global_load_lds_dwordx4 v253, s[74:75]
	s_add_i32 m0, s86, 0x400
	s_nop 0
	global_load_lds_dwordx4 v253, s[76:77]
	ds_read_b128 v[122:125], v182 offset:50688
	ds_read_b128 v[126:129], v182 offset:50752
	ds_read_b128 v[146:149], v182 offset:55040
	ds_read_b128 v[196:199], v182 offset:55104
	ds_read_b128 v[204:207], v182 offset:59392
	ds_read_b128 v[208:211], v182 offset:59456
	ds_read_b128 v[216:219], v182 offset:63744
	ds_read_b128 v[220:223], v182 offset:63808
	s_waitcnt lgkmcnt(7)
	v_mfma_f32_16x16x32_bf16 v[130:133], v[122:125], v[30:33], 0
	v_mov_b32_e32 v190, v168
	v_mov_b32_e32 v191, v158
	v_mov_b32_e32 v192, v170
	v_mfma_f32_16x16x32_bf16 v[122:125], v[122:125], v[38:41], 0
	v_mov_b32_e32 v193, v152
	v_mov_b32_e32 v152, v171
	s_lshl_b32 s8, s8, 12
	s_waitcnt lgkmcnt(5)
	v_mfma_f32_16x16x32_bf16 v[200:203], v[146:149], v[30:33], 0
	s_add_u32 s8, s42, s8
	s_addc_u32 s14, s43, 0
	s_add_u32 s12, s8, s12
	v_mfma_f32_16x16x32_bf16 v[146:149], v[146:149], v[38:41], 0
	s_addc_u32 s13, s14, s13
	s_waitcnt lgkmcnt(3)
	v_mfma_f32_16x16x32_bf16 v[212:215], v[204:207], v[30:33], 0
	s_waitcnt lgkmcnt(1)
	v_mfma_f32_16x16x32_bf16 v[30:33], v[216:219], v[30:33], 0
	v_mfma_f32_16x16x32_bf16 v[130:133], v[126:129], v[18:21], v[130:133]
	v_mfma_f32_16x16x32_bf16 v[122:125], v[126:129], v[22:25], v[122:125]
	v_mfma_f32_16x16x32_bf16 v[126:129], v[196:199], v[18:21], v[200:203]
	v_mfma_f32_16x16x32_bf16 v[146:149], v[196:199], v[22:25], v[146:149]
	v_mfma_f32_16x16x32_bf16 v[196:199], v[208:211], v[18:21], v[212:215]
	s_waitcnt lgkmcnt(0)
	v_mfma_f32_16x16x32_bf16 v[18:21], v[220:223], v[18:21], v[30:33]
	s_nop 0
	v_mov_b32_e32 v213, v156
	v_mov_b32_e32 v212, v164
	v_mov_b32_e32 v214, v166
	ds_read_b128 v[30:33], v182 offset:50816
	v_mfma_f32_16x16x32_bf16 v[204:207], v[204:207], v[38:41], 0
	v_mov_b32_e32 v215, v160
	v_mfma_f32_16x16x32_bf16 v[38:41], v[216:219], v[38:41], 0
	v_mov_b32_e32 v216, v169
	v_mov_b32_e32 v217, v159
	v_mov_b32_e32 v219, v157
	v_mfma_f32_16x16x32_bf16 v[200:203], v[208:211], v[22:25], v[204:207]
	v_mov_b32_e32 v218, v165
	v_mfma_f32_16x16x32_bf16 v[22:25], v[220:223], v[22:25], v[38:41]
	s_nop 2
	ds_read_b128 v[38:41], v182 offset:55168
	ds_read_b128 v[204:207], v182 offset:50880
	s_waitcnt lgkmcnt(2)
	v_mfma_f32_16x16x32_bf16 v[130:133], v[30:33], v[10:13], v[130:133]
	v_mfma_f32_16x16x32_bf16 v[30:33], v[30:33], v[14:17], v[122:125]
	s_nop 2
	ds_read_b128 v[122:125], v182 offset:59520
	ds_read_b128 v[208:211], v182 offset:55232
	s_waitcnt lgkmcnt(3)
	v_mfma_f32_16x16x32_bf16 v[126:129], v[38:41], v[10:13], v[126:129]
	v_mfma_f32_16x16x32_bf16 v[38:41], v[38:41], v[14:17], v[146:149]
	s_nop 2
	ds_read_b128 v[146:149], v182 offset:63872
	ds_read_b128 v[168:171], v182 offset:59584
	ds_read_b128 v[156:159], v182 offset:63936
	s_waitcnt lgkmcnt(4)
	v_mfma_f32_16x16x32_bf16 v[196:199], v[122:125], v[10:13], v[196:199]
	s_waitcnt lgkmcnt(2)
	v_mfma_f32_16x16x32_bf16 v[10:13], v[146:149], v[10:13], v[18:21]
	v_mfma_f32_16x16x32_bf16 v[122:125], v[122:125], v[14:17], v[200:203]
	s_nop 1
	v_mov_b32_e32 v18, v142
	v_mov_b32_e32 v19, v144
	v_mov_b32_e32 v20, v172
	v_mfma_f32_16x16x32_bf16 v[14:17], v[146:149], v[14:17], v[22:25]
	v_mov_b32_e32 v201, v161
	v_mov_b32_e32 v200, v167
	v_mov_b32_e32 v21, v174
	v_mfma_f32_16x16x32_bf16 v[160:163], v[204:207], v[6:9], v[30:33]
	v_add_f32_e64 v24, v190, v192
	v_add_f32_e64 v25, v191, v193
	v_mov_b32_e32 v144, v143
	v_mov_b32_e32 v22, v173
	v_pk_add_f32 v[30:31], v[212:213], v[214:215]
	v_mfma_f32_16x16x32_bf16 v[146:149], v[204:207], v[2:5], v[130:133]
	v_add_f32_e64 v24, v24, v30
	v_add_f32_e64 v25, v25, v31
	v_mov_b32_e32 v23, v175
	v_pk_add_f32 v[32:33], v[216:217], v[152:153]
	v_mfma_f32_16x16x32_bf16 v[164:167], v[208:211], v[2:5], v[126:129]
	v_add_f32_e64 v144, v144, v22
	v_add_f32_e64 v145, v145, v23
	v_add_f32_e32 v130, v134, v138
	v_add_f32_e32 v132, v136, v140
	v_mfma_f32_16x16x32_bf16 v[172:175], v[208:211], v[6:9], v[38:41]
	v_add_f32_e64 v126, v18, v20
	v_add_f32_e64 v127, v19, v21
	s_nop 0
	v_pk_add_f32 v[38:39], v[218:219], v[200:201]
	s_waitcnt lgkmcnt(1)
	v_mfma_f32_16x16x32_bf16 v[196:199], v[168:171], v[2:5], v[196:199]
	v_add_f32_e64 v142, v32, v38
	v_add_f32_e64 v143, v33, v39
	s_waitcnt lgkmcnt(0)
	v_mfma_f32_16x16x32_bf16 v[200:203], v[156:159], v[2:5], v[10:13]
	v_add_f32_e64 v2, v150, v25
	v_add_f32_e64 v3, v151, v24
	v_pk_add_f32 v[128:129], v[24:25], v[2:3]
	v_mfma_f32_16x16x32_bf16 v[168:171], v[168:171], v[6:9], v[122:125]
	s_nop 2
	v_add_f32_e32 v122, v135, v139
	v_add_f32_e32 v124, v137, v141
	v_mfma_f32_16x16x32_bf16 v[134:137], v[156:159], v[6:9], v[14:17]
	ds_read_b64_tr_b16 v[2:3], v183 offset:0
	ds_read_b64_tr_b16 v[4:5], v183 offset:0x200
	ds_read_b64_tr_b16 v[6:7], v183 offset:0x400
	ds_read_b64_tr_b16 v[8:9], v183 offset:0x600
	ds_read_b64_tr_b16 v[10:11], v183 offset:0x820
	ds_read_b64_tr_b16 v[12:13], v183 offset:0xa20
	ds_read_b64_tr_b16 v[14:15], v183 offset:0xc20
	ds_read_b64_tr_b16 v[16:17], v183 offset:0xe20
	ds_read_b64_tr_b16 v[18:19], v183 offset:0x1040
	ds_read_b64_tr_b16 v[20:21], v183 offset:0x1240
	ds_read_b64_tr_b16 v[22:23], v183 offset:0x1440
	ds_read_b64_tr_b16 v[24:25], v183 offset:0x1640
	s_waitcnt lgkmcnt(4)
	s_nop 0
	v_mfma_f32_16x16x32_bf16 v[30:33], v[2:5], v[106:109], v[102:105]
	v_mfma_f32_16x16x32_bf16 v[38:41], v[2:5], v[110:113], v[98:101]
	v_mfma_f32_16x16x32_bf16 v[94:97], v[10:13], v[106:109], v[94:97]
	v_mfma_f32_16x16x32_bf16 v[10:13], v[10:13], v[110:113], v[90:93]
	v_mfma_f32_16x16x32_bf16 v[2:5], v[6:9], v[114:117], v[30:33]
	v_mfma_f32_16x16x32_bf16 v[6:9], v[6:9], v[118:121], v[38:41]
	v_mfma_f32_16x16x32_bf16 v[38:41], v[14:17], v[114:117], v[94:97]
	v_mfma_f32_16x16x32_bf16 v[90:93], v[14:17], v[118:121], v[10:13]
	ds_read_b64_tr_b16 v[14:15], v183 offset:0x1860
	ds_read_b64_tr_b16 v[16:17], v183 offset:0x1a60
	ds_read_b64_tr_b16 v[30:31], v183 offset:0x1c60
	ds_read_b64_tr_b16 v[32:33], v183 offset:0x1e60
	s_waitcnt lgkmcnt(4)
; #define SBAR() __builtin_amdgcn_sched_barrier(0)
; #define MFMA16(a, b, c) __builtin_amdgcn_mfma_f32_16x16x32_bf16(a, b, c, 0, 0, 0)
; template <int D0> __device__ __forceinline__ void pv16(f32x4a (&o)[8][2], int vb, const bf16x8 (&pb)[2][2]) {
;     ...
;   const s16x4 a0 = TR(D0, 0, 0), a1 = TR(D0, 0, 1), a2 = TR(D0, 1, 0), a3 = TR(D0, 1, 1), b0 = TR(D0 + 1, 0, 0), b1 = TR(D0 + 1, 0, 1), b2 = TR(D0 + 1, 1, 0), b3 = TR(D0 + 1, 1, 1);
;   const s16x4 c0 = TR(D0 + 2, 0, 0), c1 = TR(D0 + 2, 0, 1), c2 = TR(D0 + 2, 1, 0), c3 = TR(D0 + 2, 1, 1);
;   asm volatile("s_waitcnt lgkmcnt(4)" ::: "memory"); SBAR();
;   o[D0][0] = MFMA16(PK16(a0, a1), pb[0][0], o[D0][0]); o[D0][1] = MFMA16(PK16(a0, a1), pb[0][1], o[D0][1]);
;   o[D0 + 1][0] = MFMA16(PK16(b0, b1), pb[0][0], o[D0 + 1][0]); o[D0 + 1][1] = MFMA16(PK16(b0, b1), pb[0][1], o[D0 + 1][1]);
;   o[D0][0] = MFMA16(PK16(a2, a3), pb[1][0], o[D0][0]); o[D0][1] = MFMA16(PK16(a2, a3), pb[1][1], o[D0][1]);
;   o[D0 + 1][0] = MFMA16(PK16(b2, b3), pb[1][0], o[D0 + 1][0]); o[D0 + 1][1] = MFMA16(PK16(b2, b3), pb[1][1], o[D0 + 1][1]);
;   SBAR();
;   const s16x4 d0 = TR(D0 + 3, 0, 0), d1 = TR(D0 + 3, 0, 1), d2 = TR(D0 + 3, 1, 0), d3 = TR(D0 + 3, 1, 1);
;   asm volatile("s_waitcnt lgkmcnt(4)" ::: "memory"); SBAR();
;   o[D0 + 2][0] = MFMA16(PK16(c0, c1), pb[0][0], o[D0 + 2][0]); o[D0 + 2][1] = MFMA16(PK16(c0, c1), pb[0][1], o[D0 + 2][1]);
;   o[D0 + 2][0] = MFMA16(PK16(c2, c3), pb[1][0], o[D0 + 2][0]); o[D0 + 2][1] = MFMA16(PK16(c2, c3), pb[1][1], o[D0 + 2][1]);
;   asm volatile("s_waitcnt lgkmcnt(0)" ::: "memory"); SBAR();
;   o[D0 + 3][0] = MFMA16(PK16(d0, d1), pb[0][0], o[D0 + 3][0]); o[D0 + 3][1] = MFMA16(PK16(d0, d1), pb[0][1], o[D0 + 3][1]);
;   o[D0 + 3][0] = MFMA16(PK16(d2, d3), pb[1][0], o[D0 + 3][0]); o[D0 + 3][1] = MFMA16(PK16(d2, d3), pb[1][1], o[D0 + 3][1]);
	v_mfma_f32_16x16x32_bf16 v[10:13], v[18:21], v[106:109], v[78:81]
	s_waitcnt lgkmcnt(0)
	v_mfma_f32_16x16x32_bf16 v[18:21], v[18:21], v[110:113], v[50:53]
	v_mfma_f32_16x16x32_bf16 v[10:13], v[22:25], v[114:117], v[10:13]
	v_mfma_f32_16x16x32_bf16 v[22:25], v[22:25], v[118:121], v[18:21]
	v_mfma_f32_16x16x32_bf16 v[18:21], v[14:17], v[106:109], v[82:85]
	v_mfma_f32_16x16x32_bf16 v[50:53], v[14:17], v[110:113], v[86:89]
	v_mfma_f32_16x16x32_bf16 v[14:17], v[30:33], v[114:117], v[18:21]
	v_mfma_f32_16x16x32_bf16 v[18:21], v[30:33], v[118:121], v[50:53]
	s_waitcnt vmcnt(0)
	s_waitcnt vmcnt(1)
	s_waitcnt vmcnt(0)
	ds_read_b64_tr_b16 v[26:27], v183 offset:0x2080
	ds_read_b64_tr_b16 v[28:29], v183 offset:0x2280
	ds_read_b64_tr_b16 v[30:31], v183 offset:0x2480
	ds_read_b64_tr_b16 v[32:33], v183 offset:0x2680
	ds_read_b64_tr_b16 v[34:35], v183 offset:0x28a0
	ds_read_b64_tr_b16 v[36:37], v183 offset:0x2aa0
	ds_read_b64_tr_b16 v[78:79], v183 offset:0x2ca0
	ds_read_b64_tr_b16 v[80:81], v183 offset:0x2ea0
	ds_read_b64_tr_b16 v[82:83], v183 offset:0x30c0
	ds_read_b64_tr_b16 v[84:85], v183 offset:0x32c0
	ds_read_b64_tr_b16 v[86:87], v183 offset:0x34c0
	ds_read_b64_tr_b16 v[88:89], v183 offset:0x36c0
	s_waitcnt lgkmcnt(4)
	s_nop 0
	v_mfma_f32_16x16x32_bf16 v[50:53], v[26:29], v[106:109], v[54:57]
	v_mfma_f32_16x16x32_bf16 v[26:29], v[26:29], v[110:113], v[62:65]
	v_mfma_f32_16x16x32_bf16 v[58:61], v[34:37], v[106:109], v[58:61]
	v_mfma_f32_16x16x32_bf16 v[34:37], v[34:37], v[110:113], v[70:73]
	v_mfma_f32_16x16x32_bf16 v[50:53], v[30:33], v[114:117], v[50:53]
	v_mfma_f32_16x16x32_bf16 v[54:57], v[30:33], v[118:121], v[26:29]
	v_mfma_f32_16x16x32_bf16 v[70:73], v[78:81], v[114:117], v[58:61]
	v_mfma_f32_16x16x32_bf16 v[78:81], v[78:81], v[118:121], v[34:37]
	ds_read_b64_tr_b16 v[30:31], v183 offset:0x38e0
	ds_read_b64_tr_b16 v[32:33], v183 offset:0x3ae0
	ds_read_b64_tr_b16 v[34:35], v183 offset:0x3ce0
	ds_read_b64_tr_b16 v[36:37], v183 offset:0x3ee0
	s_waitcnt lgkmcnt(4)
	v_mfma_f32_16x16x32_bf16 v[26:29], v[82:85], v[106:109], v[42:45]
	s_waitcnt lgkmcnt(0)
	v_mfma_f32_16x16x32_bf16 v[42:45], v[82:85], v[110:113], v[46:49]
	v_mfma_f32_16x16x32_bf16 v[26:29], v[86:89], v[114:117], v[26:29]
	v_mfma_f32_16x16x32_bf16 v[58:61], v[86:89], v[118:121], v[42:45]
	v_mfma_f32_16x16x32_bf16 v[42:45], v[30:33], v[106:109], v[66:69]
	v_mfma_f32_16x16x32_bf16 v[46:49], v[30:33], v[110:113], v[74:77]
	v_mfma_f32_16x16x32_bf16 v[30:33], v[34:37], v[114:117], v[42:45]
	v_mfma_f32_16x16x32_bf16 v[62:65], v[34:37], v[118:121], v[46:49]
	s_nop 4
	v_add_f32_e32 v42, v186, v196
	v_exp_f32_e32 v116, v42
	v_add_f32_e32 v42, v186, v197
	v_exp_f32_e32 v117, v42
	v_add_f32_e32 v42, v186, v198
	v_exp_f32_e32 v118, v42
	v_add_f32_e32 v42, v186, v199
	v_exp_f32_e32 v119, v42
	v_add_f32_e32 v42, v186, v168
	v_add_f32_e32 v34, v186, v146
	v_exp_f32_e32 v98, v42
	v_add_f32_e32 v42, v186, v169
	v_exp_f32_e32 v131, v34
	v_add_f32_e32 v34, v186, v147
	v_exp_f32_e32 v99, v42
	v_add_f32_e32 v42, v186, v170
	v_exp_f32_e32 v133, v34
	v_add_f32_e32 v34, v186, v148
	v_exp_f32_e32 v100, v42
	v_add_f32_e32 v42, v186, v171
	v_exp_f32_e32 v74, v34
	v_add_f32_e32 v34, v186, v149
	v_exp_f32_e32 v101, v42
	v_add_f32_e32 v42, v186, v200
	v_exp_f32_e32 v129, v34
	v_add_f32_e32 v34, v186, v160
	v_exp_f32_e32 v120, v42
	v_add_f32_e32 v42, v186, v201
	v_exp_f32_e32 v123, v34
	v_add_f32_e32 v34, v186, v161
	v_exp_f32_e32 v121, v42
	v_add_f32_e32 v42, v186, v202
	v_exp_f32_e32 v125, v34
	v_add_f32_e32 v34, v186, v162
	v_exp_f32_e32 v75, v42
	v_add_f32_e32 v42, v186, v203
	v_exp_f32_e32 v76, v34
	v_add_f32_e32 v34, v186, v163
	v_exp_f32_e32 v77, v42
	v_add_f32_e32 v42, v186, v134
	v_exp_f32_e32 v87, v34
	v_add_f32_e32 v34, v186, v164
	v_exp_f32_e32 v102, v42
	v_add_f32_e32 v42, v186, v135
	v_exp_f32_e32 v66, v34
	v_add_f32_e32 v34, v186, v165
	v_exp_f32_e32 v103, v42
	v_add_f32_e32 v42, v186, v136
	v_exp_f32_e32 v68, v34
	v_add_f32_e32 v34, v186, v166
	v_exp_f32_e32 v43, v42
	v_exp_f32_e32 v67, v34
	v_add_f32_e32 v34, v186, v167
	v_add_f32_e32 v35, v186, v173
	v_exp_f32_e32 v69, v34
	v_add_f32_e32 v34, v186, v172
	v_exp_f32_e32 v36, v35
	v_add_f32_e32 v35, v186, v174
	v_add_f32_e32 v37, v186, v175
	v_add_f32_e32 v42, v186, v137
	v_exp_f32_e32 v34, v34
	v_exp_f32_e32 v35, v35
	v_exp_f32_e32 v37, v37
	v_exp_f32_e32 v45, v42
	v_add_f32_e32 v42, v143, v151
	v_pk_add_f32 v[48:49], v[144:145], v[144:145] op_sel:[0,1] op_sel_hi:[1,0]
	v_pk_add_f32 v[84:85], v[142:143], v[42:43] op_sel_hi:[1,0]
	v_mov_b32_e32 v49, v76
	v_mov_b32_e32 v85, v87
	v_pk_add_f32 v[46:47], v[122:123], v[124:125]
	v_pk_add_f32 v[48:49], v[48:49], v[84:85]
	v_add_f32_e32 v42, v98, v99
	v_pk_add_f32 v[46:47], v[46:47], v[48:49]
	v_pk_add_f32 v[48:49], v[34:35], v[36:37]
	v_pk_add_f32 v[46:47], v[46:47], v[46:47] op_sel:[0,1] op_sel_hi:[1,0]
	v_pk_add_f32 v[48:49], v[48:49], v[48:49] op_sel:[0,1] op_sel_hi:[1,0]
	v_add_f32_e32 v44, v100, v101
	v_mov_b32_e32 v47, v102
	v_mov_b32_e32 v49, v103
	v_pk_add_f32 v[46:47], v[46:47], v[48:49]
	v_pk_add_f32 v[48:49], v[42:43], v[44:45]
	v_cvt_pk_bf16_f32 v82, v131, v133
	v_cvt_pk_bf16_f32 v83, v74, v129
	v_cvt_pk_bf16_f32 v84, v66, v68
	v_cvt_pk_bf16_f32 v85, v67, v69
	v_cvt_pk_bf16_f32 v86, v123, v125
	s_nop 0
	v_pk_add_f32 v[46:47], v[46:47], v[48:49]
	v_pk_add_f32 v[48:49], v[126:127], v[126:127] op_sel:[0,1] op_sel_hi:[1,0]
	v_add_f32_e32 v122, v46, v47
	v_mov_b32_e32 v49, v74
	v_pk_add_f32 v[46:47], v[130:131], v[132:133]
	v_pk_add_f32 v[48:49], v[48:49], v[128:129]
	v_cvt_pk_bf16_f32 v87, v76, v87
	v_cvt_pk_bf16_f32 v88, v34, v36
	v_cvt_pk_bf16_f32 v89, v35, v37
	v_cvt_pk_bf16_f32 v94, v116, v117
	v_cvt_pk_bf16_f32 v95, v118, v119
	s_nop 0
	v_pk_add_f32 v[114:115], v[46:47], v[48:49]
	v_cvt_pk_bf16_f32 v96, v120, v121
	v_cvt_pk_bf16_f32 v97, v75, v77
	v_cvt_pk_bf16_f32 v98, v98, v99
	v_cvt_pk_bf16_f32 v99, v100, v101
	v_cvt_pk_bf16_f32 v100, v102, v103
	v_cvt_pk_bf16_f32 v101, v43, v45
	s_waitcnt lgkmcnt(0)
	s_barrier
; #define SBAR() __builtin_amdgcn_sched_barrier(0)
; #define MFMA16(a, b, c) __builtin_amdgcn_mfma_f32_16x16x32_bf16(a, b, c, 0, 0, 0)
; template <int D0> __device__ __forceinline__ void pv16(f32x4a (&o)[8][2], int vb, const bf16x8 (&pb)[2][2]) {
;     ...
;   const s16x4 a0 = TR(D0, 0, 0), a1 = TR(D0, 0, 1), a2 = TR(D0, 1, 0), a3 = TR(D0, 1, 1), b0 = TR(D0 + 1, 0, 0), b1 = TR(D0 + 1, 0, 1), b2 = TR(D0 + 1, 1, 0), b3 = TR(D0 + 1, 1, 1);
;   const s16x4 c0 = TR(D0 + 2, 0, 0), c1 = TR(D0 + 2, 0, 1), c2 = TR(D0 + 2, 1, 0), c3 = TR(D0 + 2, 1, 1);
;   asm volatile("s_waitcnt lgkmcnt(4)" ::: "memory"); SBAR();
;   o[D0][0] = MFMA16(PK16(a0, a1), pb[0][0], o[D0][0]); o[D0][1] = MFMA16(PK16(a0, a1), pb[0][1], o[D0][1]);
;   o[D0 + 1][0] = MFMA16(PK16(b0, b1), pb[0][0], o[D0 + 1][0]); o[D0 + 1][1] = MFMA16(PK16(b0, b1), pb[0][1], o[D0 + 1][1]);
;   o[D0][0] = MFMA16(PK16(a2, a3), pb[1][0], o[D0][0]); o[D0][1] = MFMA16(PK16(a2, a3), pb[1][1], o[D0][1]);
;   o[D0 + 1][0] = MFMA16(PK16(b2, b3), pb[1][0], o[D0 + 1][0]); o[D0 + 1][1] = MFMA16(PK16(b2, b3), pb[1][1], o[D0 + 1][1]);
;   SBAR();
;   const s16x4 d0 = TR(D0 + 3, 0, 0), d1 = TR(D0 + 3, 0, 1), d2 = TR(D0 + 3, 1, 0), d3 = TR(D0 + 3, 1, 1);
;   asm volatile("s_waitcnt lgkmcnt(4)" ::: "memory"); SBAR();
;   o[D0 + 2][0] = MFMA16(PK16(c0, c1), pb[0][0], o[D0 + 2][0]); o[D0 + 2][1] = MFMA16(PK16(c0, c1), pb[0][1], o[D0 + 2][1]);
;   o[D0 + 2][0] = MFMA16(PK16(c2, c3), pb[1][0], o[D0 + 2][0]); o[D0 + 2][1] = MFMA16(PK16(c2, c3), pb[1][1], o[D0 + 2][1]);
;   asm volatile("s_waitcnt lgkmcnt(0)" ::: "memory"); SBAR();
;   o[D0 + 3][0] = MFMA16(PK16(d0, d1), pb[0][0], o[D0 + 3][0]); o[D0 + 3][1] = MFMA16(PK16(d0, d1), pb[0][1], o[D0 + 3][1]);
;   o[D0 + 3][0] = MFMA16(PK16(d2, d3), pb[1][0], o[D0 + 3][0]); o[D0 + 3][1] = MFMA16(PK16(d2, d3), pb[1][1], o[D0 + 3][1]);
; template <int LDQ, int LDK, int LDO>
; __device__ __forceinline__ void attn_gqa16_body(const bf16* __restrict__ Qb, const bf16* __restrict__ Kh, const bf16* __restrict__ Vh, bf16* __restrict__ Ob, int seq, char* lds, float mref) {
;     ...
;   __builtin_amdgcn_s_setprio(0);
;   ls0 += __shfl_xor(ls0, 16); ls0 += __shfl_xor(ls0, 32); ls1 += __shfl_xor(ls1, 16); ls1 += __shfl_xor(ls1, 32);
;   const float rl[2] = {__builtin_amdgcn_rcpf(ls0), __builtin_amdgcn_rcpf(ls1)};
	ds_read_b64_tr_b16 v[34:35], v184 offset:0
	ds_read_b64_tr_b16 v[36:37], v184 offset:0x200
	ds_read_b64_tr_b16 v[42:43], v184 offset:0x400
	ds_read_b64_tr_b16 v[44:45], v184 offset:0x600
	ds_read_b64_tr_b16 v[46:47], v184 offset:0x820
	ds_read_b64_tr_b16 v[48:49], v184 offset:0xa20
	ds_read_b64_tr_b16 v[102:103], v184 offset:0xc20
	ds_read_b64_tr_b16 v[104:105], v184 offset:0xe20
	ds_read_b64_tr_b16 v[106:107], v184 offset:0x1040
	ds_read_b64_tr_b16 v[108:109], v184 offset:0x1240
	ds_read_b64_tr_b16 v[110:111], v184 offset:0x1440
	ds_read_b64_tr_b16 v[112:113], v184 offset:0x1640
	s_waitcnt lgkmcnt(4)
	s_nop 0
	v_mfma_f32_16x16x32_bf16 v[2:5], v[34:37], v[82:85], v[2:5]
	v_mfma_f32_16x16x32_bf16 v[6:9], v[34:37], v[86:89], v[6:9]
	v_mfma_f32_16x16x32_bf16 v[34:37], v[46:49], v[82:85], v[38:41]
	v_mfma_f32_16x16x32_bf16 v[46:49], v[46:49], v[86:89], v[90:93]
	v_mfma_f32_16x16x32_bf16 v[38:41], v[42:45], v[94:97], v[2:5]
	v_mfma_f32_16x16x32_bf16 v[6:9], v[42:45], v[98:101], v[6:9]
	v_mfma_f32_16x16x32_bf16 v[34:37], v[102:105], v[94:97], v[34:37]
	v_mfma_f32_16x16x32_bf16 v[2:5], v[102:105], v[98:101], v[46:49]
	ds_read_b64_tr_b16 v[46:47], v184 offset:0x1860
	ds_read_b64_tr_b16 v[48:49], v184 offset:0x1a60
	ds_read_b64_tr_b16 v[90:91], v184 offset:0x1c60
	ds_read_b64_tr_b16 v[92:93], v184 offset:0x1e60
	s_waitcnt lgkmcnt(4)
	v_mfma_f32_16x16x32_bf16 v[10:13], v[106:109], v[82:85], v[10:13]
	s_waitcnt lgkmcnt(0)
	v_mfma_f32_16x16x32_bf16 v[22:25], v[106:109], v[86:89], v[22:25]
	v_mfma_f32_16x16x32_bf16 v[42:45], v[110:113], v[94:97], v[10:13]
	v_mfma_f32_16x16x32_bf16 v[10:13], v[110:113], v[98:101], v[22:25]
	v_mfma_f32_16x16x32_bf16 v[14:17], v[46:49], v[82:85], v[14:17]
	v_mfma_f32_16x16x32_bf16 v[18:21], v[46:49], v[86:89], v[18:21]
	v_mfma_f32_16x16x32_bf16 v[46:49], v[90:93], v[94:97], v[14:17]
	v_mfma_f32_16x16x32_bf16 v[14:17], v[90:93], v[98:101], v[18:21]
	s_waitcnt vmcnt(0)
	ds_read_b64_tr_b16 v[18:19], v184 offset:0x2080
	ds_read_b64_tr_b16 v[20:21], v184 offset:0x2280
	ds_read_b64_tr_b16 v[22:23], v184 offset:0x2480
	ds_read_b64_tr_b16 v[24:25], v184 offset:0x2680
	ds_read_b64_tr_b16 v[90:91], v184 offset:0x28a0
	ds_read_b64_tr_b16 v[92:93], v184 offset:0x2aa0
	ds_read_b64_tr_b16 v[102:103], v184 offset:0x2ca0
	ds_read_b64_tr_b16 v[104:105], v184 offset:0x2ea0
	ds_read_b64_tr_b16 v[106:107], v184 offset:0x30c0
	ds_read_b64_tr_b16 v[108:109], v184 offset:0x32c0
	ds_read_b64_tr_b16 v[110:111], v184 offset:0x34c0
	ds_read_b64_tr_b16 v[112:113], v184 offset:0x36c0
	s_waitcnt lgkmcnt(4)
	s_nop 5
	v_mfma_f32_16x16x32_bf16 v[50:53], v[18:21], v[82:85], v[50:53]
	v_mfma_f32_16x16x32_bf16 v[18:21], v[18:21], v[86:89], v[54:57]
	v_mfma_f32_16x16x32_bf16 v[70:73], v[90:93], v[82:85], v[70:73]
	v_mfma_f32_16x16x32_bf16 v[78:81], v[90:93], v[86:89], v[78:81]
	v_mfma_f32_16x16x32_bf16 v[54:57], v[22:25], v[94:97], v[50:53]
	v_mfma_f32_16x16x32_bf16 v[22:25], v[22:25], v[98:101], v[18:21]
	v_mfma_f32_16x16x32_bf16 v[50:53], v[102:105], v[94:97], v[70:73]
	v_mfma_f32_16x16x32_bf16 v[18:21], v[102:105], v[98:101], v[78:81]
	ds_read_b64_tr_b16 v[70:71], v184 offset:0x38e0
	ds_read_b64_tr_b16 v[72:73], v184 offset:0x3ae0
	ds_read_b64_tr_b16 v[78:79], v184 offset:0x3ce0
	ds_read_b64_tr_b16 v[80:81], v184 offset:0x3ee0
	s_waitcnt lgkmcnt(4)
	v_mfma_f32_16x16x32_bf16 v[26:29], v[106:109], v[82:85], v[26:29]
	s_waitcnt lgkmcnt(0)
	v_mfma_f32_16x16x32_bf16 v[90:93], v[106:109], v[86:89], v[58:61]
	v_mfma_f32_16x16x32_bf16 v[58:61], v[110:113], v[94:97], v[26:29]
	v_mfma_f32_16x16x32_bf16 v[26:29], v[110:113], v[98:101], v[90:93]
	v_mfma_f32_16x16x32_bf16 v[30:33], v[70:73], v[82:85], v[30:33]
	v_mfma_f32_16x16x32_bf16 v[70:73], v[70:73], v[86:89], v[62:65]
	v_mfma_f32_16x16x32_bf16 v[62:65], v[78:81], v[94:97], v[30:33]
	v_mfma_f32_16x16x32_bf16 v[30:33], v[78:81], v[98:101], v[70:73]
	v_add_f32_e64 v66, v66, v68
	v_add_f32_e64 v67, v67, v69
	v_pk_add_f32 v[68:69], v[114:115], v[114:115] op_sel:[0,1] op_sel_hi:[1,0]
	v_pk_add_f32 v[66:67], v[66:67], v[66:67] op_sel:[0,1] op_sel_hi:[1,0]
	v_add_f32_e32 v74, v116, v117
	v_add_f32_e32 v76, v118, v119
	v_mov_b32_e32 v69, v120
	v_mov_b32_e32 v67, v121
	v_pk_add_f32 v[66:67], v[68:69], v[66:67]
	v_pk_add_f32 v[68:69], v[74:75], v[76:77]
	s_nop 0
	v_pk_add_f32 v[66:67], v[66:67], v[68:69]
	s_nop 0
	v_add_f32_e32 v66, v66, v67
	s_setprio 0
	ds_bpermute_b32 v67, v177, v66
	ds_bpermute_b32 v68, v177, v122
	v_mov_b32_e32 v70, v185
	s_waitcnt lgkmcnt(1)
	v_add_f32_e32 v66, v66, v67
	s_waitcnt lgkmcnt(0)
	v_add_f32_e32 v67, v122, v68
	ds_bpermute_b32 v68, v188, v66
	ds_bpermute_b32 v69, v188, v67
	s_waitcnt lgkmcnt(1)
	v_add_f32_e32 v66, v66, v68
	s_waitcnt lgkmcnt(0)
	v_add_f32_e32 v67, v67, v69
	v_rcp_f32_e32 v68, v66
	v_rcp_f32_e32 v66, v67
	v_mov_b32_e32 v67, v176
	v_mov_b32_e32 v69, v180
	s_branch .LBB0_641
